# v043 with the GEMM1 start stagger reduced from 4 groups to 2 groups
# baseline (speedup 1.0000x reference)
.LBB0_1235:
	s_andn2_b64 vcc, exec, s[0:1]
	s_cbranch_vccnz .LBB0_1338
	s_cmp_lg_u32 s52, 3
	v_readlane_b32 s4, v253, 4
	s_cselect_b64 s[0:1], -1, 0
	v_readlane_b32 s5, v253, 5
	s_and_b64 s[0:1], s[4:5], s[0:1]
	v_readlane_b32 s4, v254, 32
	v_readlane_b32 s5, v254, 33
	s_and_b64 s[4:5], s[4:5], s[0:1]
	v_readlane_b32 s44, v253, 0
	v_readlane_b32 s45, v253, 1
	s_andn2_b64 vcc, exec, s[4:5]
	s_mov_b64 s[4:5], -1
	s_cbranch_vccz .LBB0_1258
	v_mov_b32_e32 v4, v0
	s_movk_i32 s5, 0x3c0
	v_readfirstlane_b32 s23, v4
	v_and_b32_e32 v2, 48, v4
	v_lshlrev_b32_e32 v3, 6, v4
	s_ashr_i32 s25, s23, 8
	v_and_or_b32 v2, v3, s5, v2
	v_lshlrev_b32_e32 v3, 2, v4
	s_ashr_i32 s24, s23, 6
	s_lshl_b32 s4, s25, 13
	v_and_b32_e32 v5, 32, v3
	v_bitop3_b32 v3, v2, s4, v5 bitop3:0xde
	s_lshl_b32 s4, s24, 5
	s_and_b32 s6, s4, 0x60
	s_lshl_b32 s4, s6, 7
	v_bitop3_b32 v2, s4, v2, v5 bitop3:0xf6
	v_readlane_b32 s4, v254, 34
	v_readlane_b32 s5, v254, 35
	v_or_b32_e32 v2, 0x10000, v2
	s_andn2_b64 vcc, exec, s[4:5]
	s_cbranch_vccnz .LBB0_1257
	s_cmp_lt_u32 s52, 3
	s_cbranch_scc0 .Lfz_nostag
	s_bfe_u32 s4, s88, 0x10003
	s_cmp_eq_u32 s4, 0
	s_cbranch_scc1 .Lfz_nostag
